# speedup vs baseline: 1.0171x; 1.0171x over previous
.Llg_join:
	v_add_f32_e32 v16, v16, v24
	v_add_f32_e32 v32, v32, v40
	v_add_f32_e32 v17, v17, v25
	v_add_f32_e32 v33, v33, v41
	v_add_f32_e32 v18, v18, v26
	v_add_f32_e32 v34, v34, v42
	v_add_f32_e32 v19, v19, v27
	v_add_f32_e32 v35, v35, v43
	v_add_f32_e32 v20, v20, v28
	v_add_f32_e32 v36, v36, v44
	v_add_f32_e32 v21, v21, v29
	v_add_f32_e32 v37, v37, v45
	v_add_f32_e32 v22, v22, v30
	v_add_f32_e32 v38, v38, v46
	v_add_f32_e32 v23, v23, v31
	v_add_f32_e32 v39, v39, v47
	v_add_f32_e32 v16, v16, v32
	v_add_f32_e32 v17, v17, v33
	v_add_f32_e32 v18, v18, v34
	v_add_f32_e32 v19, v19, v35
	v_add_f32_e32 v20, v20, v36
	v_add_f32_e32 v21, v21, v37
	v_add_f32_e32 v22, v22, v38
	v_add_f32_e32 v23, v23, v39
	v_mul_f32_e32 v16, v16, v48
	v_mul_f32_e32 v17, v17, v49
	v_mul_f32_e32 v18, v18, v50
	v_mul_f32_e32 v19, v19, v51
	v_mul_f32_e32 v20, v20, v52
	v_mul_f32_e32 v21, v21, v53
	v_mul_f32_e32 v22, v22, v54
	v_mul_f32_e32 v23, v23, v55
	v_max3_f32 v56, v16, v17, v18
	v_max3_f32 v57, v19, v20, v21
	v_max3_f32 v56, v56, v22, v23
	v_max_f32_e32 v56, v56, v57
	v_mov_b32_e32 v58, 0xff800000
	v_cmp_eq_u32_e32 vcc, 0, v10
	s_nop 1
	v_cndmask_b32_e32 v58, v58, v16, vcc
	v_cmp_eq_u32_e32 vcc, 1, v10
	s_nop 1
	v_cndmask_b32_e32 v58, v58, v17, vcc
	v_cmp_eq_u32_e32 vcc, 2, v10
	s_nop 1
	v_cndmask_b32_e32 v58, v58, v18, vcc
	v_cmp_eq_u32_e32 vcc, 3, v10
	s_nop 1
	v_cndmask_b32_e32 v58, v58, v19, vcc
	v_cmp_eq_u32_e32 vcc, 4, v10
	s_nop 1
	v_cndmask_b32_e32 v58, v58, v20, vcc
	v_cmp_eq_u32_e32 vcc, 5, v10
	s_nop 1
	v_cndmask_b32_e32 v58, v58, v21, vcc
	v_cmp_eq_u32_e32 vcc, 6, v10
	s_nop 1
	v_cndmask_b32_e32 v58, v58, v22, vcc
	v_cmp_eq_u32_e32 vcc, 7, v10
	s_nop 1
	v_cndmask_b32_e32 v58, v58, v23, vcc
	s_nop 1
	v_max_f32_dpp v57, v56, v56 quad_perm:[1,0,3,2] row_mask:0xf bank_mask:0xf
	s_nop 1
	v_max_f32_dpp v56, v57, v57 quad_perm:[2,3,0,1] row_mask:0xf bank_mask:0xf
	s_nop 0
	v_sub_f32_e32 v24, v16, v56
	v_sub_f32_e32 v25, v17, v56
	v_sub_f32_e32 v26, v18, v56
	v_sub_f32_e32 v27, v19, v56
	v_sub_f32_e32 v28, v20, v56
	v_sub_f32_e32 v29, v21, v56
	v_sub_f32_e32 v30, v22, v56
	v_sub_f32_e32 v31, v23, v56
	v_mul_f32_e32 v24, 0x3fb8aa3b, v24
	v_mul_f32_e32 v25, 0x3fb8aa3b, v25
	v_mul_f32_e32 v26, 0x3fb8aa3b, v26
	v_mul_f32_e32 v27, 0x3fb8aa3b, v27
	v_mul_f32_e32 v28, 0x3fb8aa3b, v28
	v_mul_f32_e32 v29, 0x3fb8aa3b, v29
	v_mul_f32_e32 v30, 0x3fb8aa3b, v30
	v_mul_f32_e32 v31, 0x3fb8aa3b, v31
	v_exp_f32_e32 v24, v24
	v_exp_f32_e32 v25, v25
	v_exp_f32_e32 v26, v26
	v_exp_f32_e32 v27, v27
	v_exp_f32_e32 v28, v28
	v_exp_f32_e32 v29, v29
	v_exp_f32_e32 v30, v30
	v_exp_f32_e32 v31, v31
	s_nop 0
	v_add_f32_e32 v24, v24, v25
	v_add_f32_e32 v26, v26, v27
	v_add_f32_e32 v28, v28, v29
	v_add_f32_e32 v30, v30, v31
	v_add_f32_e32 v24, v24, v26
	v_add_f32_e32 v28, v28, v30
	v_add_f32_e32 v59, v24, v28
	s_nop 1
	v_add_f32_dpp v60, v59, v59 quad_perm:[1,0,3,2] row_mask:0xf bank_mask:0xf
	v_max_f32_dpp v61, v58, v58 quad_perm:[1,0,3,2] row_mask:0xf bank_mask:0xf
	s_nop 1
	v_add_f32_dpp v57, v60, v60 quad_perm:[2,3,0,1] row_mask:0xf bank_mask:0xf
	v_max_f32_dpp v58, v61, v61 quad_perm:[2,3,0,1] row_mask:0xf bank_mask:0xf
	v_log_f32_e32 v57, v57
	v_cmp_eq_u32_e32 vcc, 0, v7
	v_mul_f32_e32 v57, 0x3f317217, v57
	v_add_f32_e32 v56, v56, v57
	s_and_saveexec_b64 s[4:5], vcc
	s_cbranch_execz .Llg_end
	s_cmpk_ge_u32 s30, 0x80
	s_cbranch_scc1 .Llg_st1
	s_lshl_b32 s8, s3, 9
	s_lshl_b32 s9, s10, 5
	s_add_i32 s8, s8, s9
	v_add_u32_e32 v2, s8, v6
	v_lshlrev_b32_e32 v2, 2, v2
	global_store_dword v2, v56, s[24:25]
	s_cmp_lg_u32 s10, s3
	s_cbranch_scc1 .Llg_end
	v_add_u32_e32 v3, s9, v6
	v_lshlrev_b32_e32 v3, 2, v3
	global_store_dword v3, v58, s[28:29]
	s_branch .Llg_end
.Llg_st1:
	s_lshl_b32 s8, s10, 9
	s_lshl_b32 s9, s3, 5
	s_add_i32 s8, s8, s9
	v_add_u32_e32 v2, s8, v6
	v_lshlrev_b32_e32 v2, 2, v2
	global_store_dword v2, v56, s[26:27]
	s_cmp_lg_u32 s10, 0
	s_cbranch_scc1 .Llg_end
	v_lshlrev_b32_e32 v4, 2, v6
	ds_read_b32 v5, v4 offset:16896
	v_add_u32_e32 v3, s9, v6
	v_lshlrev_b32_e32 v3, 2, v3
	s_waitcnt lgkmcnt(0)
	global_store_dword v3, v5, s[28:29] offset:2048

_Z12final_kernelPKDv4_fS1_PKfS3_Pf:
	s_load_dwordx4 s[4:7], s[0:1], 0x0
	s_load_dwordx2 s[2:3], s[0:1], 0x10
	s_load_dwordx2 s[8:9], s[0:1], 0x20
	v_and_b32_e32 v1, 0x1ff, v0
	v_readfirstlane_b32 s10, v0
	v_lshlrev_b32_e32 v3, 2, v1
	v_add_u32_e32 v4, 0x1000, v3
	v_add_u32_e32 v5, 0x2000, v3
	v_add_u32_e32 v6, 0x3000, v3
	v_add_u32_e32 v7, 0x4000, v3
	v_add_u32_e32 v8, 0x5000, v3
	v_add_u32_e32 v9, 0x6000, v3
	v_add_u32_e32 v10, 0x7000, v3
	s_cmpk_ge_u32 s10, 0x200
	s_waitcnt lgkmcnt(0)
	s_cselect_b32 s4, s6, s4
	s_cselect_b32 s5, s7, s5
	global_load_dword v12, v3, s[4:5] nt
	global_load_dword v13, v3, s[4:5] offset:2048 nt
	global_load_dword v14, v4, s[4:5] nt
	global_load_dword v15, v4, s[4:5] offset:2048 nt
	global_load_dword v16, v5, s[4:5] nt
	global_load_dword v17, v5, s[4:5] offset:2048 nt
	global_load_dword v18, v6, s[4:5] nt
	global_load_dword v19, v6, s[4:5] offset:2048 nt
	global_load_dword v20, v7, s[4:5] nt
	global_load_dword v21, v7, s[4:5] offset:2048 nt
	global_load_dword v22, v8, s[4:5] nt
	global_load_dword v23, v8, s[4:5] offset:2048 nt
	global_load_dword v24, v9, s[4:5] nt
	global_load_dword v25, v9, s[4:5] offset:2048 nt
	global_load_dword v26, v10, s[4:5] nt
	global_load_dword v27, v10, s[4:5] offset:2048 nt
	global_load_dword v44, v3, s[2:3] nt
	global_load_dword v45, v3, s[2:3] offset:2048 nt
	s_waitcnt vmcnt(2)
	v_max3_f32 v46, v12, v13, v14
	v_max3_f32 v47, v15, v16, v17
	v_max3_f32 v48, v18, v19, v20
	v_max3_f32 v49, v21, v22, v23
	v_max3_f32 v46, v46, v24, v25
	v_max3_f32 v47, v47, v26, v27
	v_max3_f32 v46, v46, v48, v49
	v_max_f32_e32 v46, v46, v47
	v_sub_f32_e32 v12, v12, v46
	v_sub_f32_e32 v13, v13, v46
	v_sub_f32_e32 v14, v14, v46
	v_sub_f32_e32 v15, v15, v46
	v_sub_f32_e32 v16, v16, v46
	v_sub_f32_e32 v17, v17, v46
	v_sub_f32_e32 v18, v18, v46
	v_sub_f32_e32 v19, v19, v46
	v_sub_f32_e32 v20, v20, v46
	v_sub_f32_e32 v21, v21, v46
	v_sub_f32_e32 v22, v22, v46
	v_sub_f32_e32 v23, v23, v46
	v_sub_f32_e32 v24, v24, v46
	v_sub_f32_e32 v25, v25, v46
	v_sub_f32_e32 v26, v26, v46
	v_sub_f32_e32 v27, v27, v46
	v_mul_f32_e32 v12, 0x3fb8aa3b, v12
	v_mul_f32_e32 v13, 0x3fb8aa3b, v13
	v_mul_f32_e32 v14, 0x3fb8aa3b, v14
	v_mul_f32_e32 v15, 0x3fb8aa3b, v15
	v_mul_f32_e32 v16, 0x3fb8aa3b, v16
	v_mul_f32_e32 v17, 0x3fb8aa3b, v17
	v_mul_f32_e32 v18, 0x3fb8aa3b, v18
	v_mul_f32_e32 v19, 0x3fb8aa3b, v19
	v_mul_f32_e32 v20, 0x3fb8aa3b, v20
	v_mul_f32_e32 v21, 0x3fb8aa3b, v21
	v_mul_f32_e32 v22, 0x3fb8aa3b, v22
	v_mul_f32_e32 v23, 0x3fb8aa3b, v23
	v_mul_f32_e32 v24, 0x3fb8aa3b, v24
	v_mul_f32_e32 v25, 0x3fb8aa3b, v25
	v_mul_f32_e32 v26, 0x3fb8aa3b, v26
	v_mul_f32_e32 v27, 0x3fb8aa3b, v27
	v_exp_f32_e32 v12, v12
	v_exp_f32_e32 v13, v13
	v_exp_f32_e32 v14, v14
	v_exp_f32_e32 v15, v15
	v_exp_f32_e32 v16, v16
	v_exp_f32_e32 v17, v17
	v_exp_f32_e32 v18, v18
	v_exp_f32_e32 v19, v19
	v_exp_f32_e32 v20, v20
	v_exp_f32_e32 v21, v21
	v_exp_f32_e32 v22, v22
	v_exp_f32_e32 v23, v23
	v_exp_f32_e32 v24, v24
	v_exp_f32_e32 v25, v25
	v_exp_f32_e32 v26, v26
	v_exp_f32_e32 v27, v27
	s_nop 0
	v_add_f32_e32 v12, v12, v20
	v_add_f32_e32 v13, v13, v21
	v_add_f32_e32 v14, v14, v22
	v_add_f32_e32 v15, v15, v23
	v_add_f32_e32 v16, v16, v24
	v_add_f32_e32 v17, v17, v25
	v_add_f32_e32 v18, v18, v26
	v_add_f32_e32 v19, v19, v27
	v_add_f32_e32 v12, v12, v16
	v_add_f32_e32 v13, v13, v17
	v_add_f32_e32 v14, v14, v18
	v_add_f32_e32 v15, v15, v19
	v_add_f32_e32 v12, v12, v14
	v_add_f32_e32 v13, v13, v15
	v_add_f32_e32 v47, v12, v13
	v_log_f32_e32 v47, v47
	s_mov_b32 s11, 0x3f317217
	v_mul_f32_e32 v48, 0x3f317217, v47
	v_fma_f32 v48, v47, s11, -v48
	v_fmamk_f32 v48, v47, 0x3377d1cf, v48
	v_fmac_f32_e32 v48, 0x3f317217, v47
	v_add_f32_e32 v46, v46, v48
	s_waitcnt vmcnt(0)
	v_sub_f32_e32 v46, v46, v44
	v_cmp_lt_f32_e32 vcc, 0, v45
	s_nop 1
	v_cndmask_b32_e32 v46, 0, v46, vcc
	v_cmp_lt_f32_e32 vcc, 0, v46
	v_max_f32_e32 v2, 0, v46
	s_nop 0
	v_cndmask_b32_e64 v3, 0, 1.0, vcc
	s_nop 0
	s_nop 0
	v_add_f32_dpp v2, v2, v2 quad_perm:[1,0,3,2] row_mask:0xf bank_mask:0xf
	v_add_f32_dpp v3, v3, v3 quad_perm:[1,0,3,2] row_mask:0xf bank_mask:0xf
	s_nop 0
	v_add_f32_dpp v2, v2, v2 quad_perm:[2,3,0,1] row_mask:0xf bank_mask:0xf
	v_add_f32_dpp v3, v3, v3 quad_perm:[2,3,0,1] row_mask:0xf bank_mask:0xf
	s_nop 0
	v_add_f32_dpp v2, v2, v2 row_half_mirror row_mask:0xf bank_mask:0xf
	v_add_f32_dpp v3, v3, v3 row_half_mirror row_mask:0xf bank_mask:0xf
	s_nop 0
	v_add_f32_dpp v2, v2, v2 row_mirror row_mask:0xf bank_mask:0xf
	v_add_f32_dpp v3, v3, v3 row_mirror row_mask:0xf bank_mask:0xf
	s_nop 0
	v_add_f32_dpp v2, v2, v2 row_bcast:15 row_mask:0xa bank_mask:0xf
	v_add_f32_dpp v3, v3, v3 row_bcast:15 row_mask:0xa bank_mask:0xf
	s_nop 0
	v_add_f32_dpp v2, v2, v2 row_bcast:31 row_mask:0xc bank_mask:0xf
	v_add_f32_dpp v3, v3, v3 row_bcast:31 row_mask:0xc bank_mask:0xf
	s_nop 1
	v_readlane_b32 s12, v2, 63
	v_readlane_b32 s13, v3, 63
	s_lshr_b32 s10, s10, 6
	s_lshl_b32 s10, s10, 2
	v_mov_b32_e32 v4, s10
	v_mov_b32_e32 v5, s12
	v_mov_b32_e32 v6, s13
	ds_write2_b32 v4, v5, v6 offset1:16
	s_waitcnt lgkmcnt(0)
	s_barrier
	s_cmp_lg_u32 s10, 0
	s_cbranch_scc1 .Lfin_end
	v_and_b32_e32 v4, 15, v0
	v_lshlrev_b32_e32 v4, 2, v4
	ds_read2_b32 v[2:3], v4 offset1:16
	s_waitcnt lgkmcnt(0)
	s_nop 0
	s_nop 0
	v_add_f32_dpp v2, v2, v2 quad_perm:[1,0,3,2] row_mask:0xf bank_mask:0xf
	v_add_f32_dpp v3, v3, v3 quad_perm:[1,0,3,2] row_mask:0xf bank_mask:0xf
	s_nop 0
	v_add_f32_dpp v2, v2, v2 quad_perm:[2,3,0,1] row_mask:0xf bank_mask:0xf
	v_add_f32_dpp v3, v3, v3 quad_perm:[2,3,0,1] row_mask:0xf bank_mask:0xf
	s_nop 0
	v_add_f32_dpp v2, v2, v2 row_half_mirror row_mask:0xf bank_mask:0xf
	v_add_f32_dpp v3, v3, v3 row_half_mirror row_mask:0xf bank_mask:0xf
	v_max_f32_e32 v5, 1.0, v3
	v_div_scale_f32 v6, s[12:13], v5, v5, v2
	v_rcp_f32_e32 v7, v6
	v_div_scale_f32 v8, vcc, v2, v5, v2
	v_fma_f32 v9, -v6, v7, 1.0
	v_fmac_f32_e32 v7, v9, v7
	v_mul_f32_e32 v9, v8, v7
	v_fma_f32 v10, -v6, v9, v8
	v_fmac_f32_e32 v9, v10, v7
	v_fma_f32 v6, -v6, v9, v8
	v_div_fmas_f32 v6, v6, v7, v9
	v_div_fixup_f32 v6, v6, v5, v2
	v_cmp_lt_f32_e32 vcc, 0, v3
	s_nop 1
	v_cndmask_b32_e32 v6, 0, v6, vcc
	s_nop 1
	v_add_f32_dpp v7, v6, v6 row_shl:8 row_mask:0xf bank_mask:0xf
	v_mov_b32_e32 v8, 0
	v_mul_f32_e32 v7, 0.5, v7
	v_cmp_eq_u32_e32 vcc, 0, v0
	s_and_saveexec_b64 s[12:13], vcc
	global_store_dword v8, v7, s[8:9]
